# accumulator zero-init via two MFMAs with a zero B operand instead of 16 v_mov_b64
# baseline (speedup 1.0000x reference)
.LBB1_82:
	v_mov_b64_e32 v[4:5], 0
	v_mov_b64_e32 v[6:7], 0
	s_nop 1
	v_mfma_f32_32x32x16_f16 v[98:113], v[194:197], v[4:7], 0
	v_mfma_f32_32x32x16_f16 v[82:97], v[194:197], v[4:7], 0
	v_cmp_lt_f32_e32 vcc, v244, v243
	s_cbranch_vccnz .LBB1_22
	s_branch .LBB1_23
